# L0 mixer conversion slots: column-maxima item issues its 16 row loads together (one wait) instead of 8 serialized load pairs
# speedup vs baseline: 1.0195x; 1.0077x over previous
; __device__ __forceinline__ void colmax_item(const float* src, int ld, int k0, int c0, float* cmx  , int lane) {
;     const int c = lane & 7, q = lane >> 3;
;     f32x4 mx = (f32x4){0.f, 0.f, 0.f, 0.f};
; #pragma unroll
;     for (int g = 0; g < 4; ++g)
; #pragma unroll
;         for (int j = 0; j < 4; ++j) { const f32x4 v = *(const f32x4*)(src + (size_t)(k0 + 32 * g + 4 * q + j) * ld + c0 + 4 * c);
;             mx[0] = fmaxf(mx[0], fabsf(v[0])); mx[1] = fmaxf(mx[1], fabsf(v[1])); mx[2] = fmaxf(mx[2], fabsf(v[2])); mx[3] = fmaxf(mx[3], fabsf(v[3])); }
; #pragma unroll
;     for (int i = 0; i < 4; ++i) { float v = mx[i]; v = fmaxf(v, __shfl_xor(v, 8)); v = fmaxf(v, __shfl_xor(v, 16)); v = fmaxf(v, __shfl_xor(v, 32)); mx[i] = v; }
;     if (q == 0) {
; #pragma unroll
;         for (int i = 0; i < 4; ++i) atomicMax((unsigned*)(cmx + 4 * c + i), __float_as_uint(mx[i] * CMS_F)); }
; }
; template <int GRP>
; __device__ __forceinline__ void conv_item(Frame& F, int r) {
;     ...
;     else { constexpr int KBN = (GRP == 3) ? 16 : CMS_KB, I_E = KBN * 88; const int up = r / (8 * I_E); r %= (8 * I_E); const int e = r / I_E; r %= I_E; const int kb = r / 88, nb = r % 88, n0 = nb * 32, drow = (n0 >> 7) * 256 + up * 128 + (n0 & 127);
;         if (GRP == 3) cvt_item_i8(inptr(F, up ? IN_MU : IN_MG) + (size_t)e * D * DFE, DFE, kb * 128, n0, ws + WS_MGU + (size_t)e * 2 * DFE * D, D, drow, cmx + 2 * DFF + e * 2 * DFE + drow, scr, F.lane);
;         else colmax_item(inptr(F, up ? IN_MU : IN_MG) + (size_t)e * D * DFE, DFE, kb * 128, n0, cmx + 2 * DFF + e * 2 * DFE + drow, F.lane); }
.LBB0_514:
	s_cmpk_gt_i32 s20, 0x3ff
	s_mov_b64 s[16:17], -1
	s_cbranch_scc0 .LBB0_522
	s_cmpk_gt_u32 s20, 0x2fff
	s_cbranch_scc0 .LBB0_519
	s_add_i32 s8, s20, 0xffffd000
	s_add_i32 s16, s20, 0xca80
	s_cmpk_lt_u32 s8, 0x580
	s_cselect_b32 s16, s8, s16
	s_and_b32 s17, s16, 0xffff
	s_mul_i32 s17, s17, 0xba2f
	s_lshr_b32 s21, s17, 23
	s_mul_i32 s17, s21, 0xb0
	s_sub_i32 s16, s16, s17
	s_and_b32 s17, s16, 0xffff
	s_add_i32 s16, s17, 0xffffffa8
	s_min_u32 s69, s17, s16
	s_lshl_b32 s16, s69, 5
	s_cmpk_lt_u32 s20, 0x3580
	s_cselect_b32 s18, s25, 0xa8
	s_add_i32 s18, s18, 0
	s_add_i32 s18, s18, 0x20200
	v_mov_b32_e32 v1, s18
	s_waitcnt lgkmcnt(3)
	ds_read_b64 v[2:3], v1
	s_cmpk_gt_u32 s17, 0x57
	s_cselect_b32 s17, 0x80, 0
	v_or_b32_e32 v1, s17, v15
	s_ashr_i32 s17, s16, 31
	s_waitcnt lgkmcnt(0)
	v_readfirstlane_b32 s18, v2
	v_readfirstlane_b32 s19, v3
	v_mul_u32_u24_e32 v2, s21, v35
	v_mov_b32_e32 v3, v11
	v_lshlrev_b64 v[2:3], 2, v[2:3]
	v_lshl_add_u64 v[2:3], s[18:19], 0, v[2:3]
	s_lshl_b64 s[18:19], s[16:17], 2
	v_lshl_add_u64 v[2:3], v[2:3], 0, s[18:19]
	v_lshl_add_u64 v[2:3], v[2:3], 0, v[10:11]
	v_mul_u32_u24_e32 v4, 0x2c00, v1
	v_mov_b32_e32 v5, v11
	v_lshl_add_u64 v[2:3], v[2:3], 0, v[4:5]
	global_load_dwordx4 v[4:7], v[2:3], off
	v_mad_u64_u32 v[38:39], vcc, s26, 1, v[2:3]
	global_load_dwordx4 v[38:41], v[38:39], off offset:3072
	v_mad_u64_u32 v[42:43], vcc, s27, 1, v[2:3]
	global_load_dwordx4 v[42:45], v[42:43], off offset:2048
	v_mad_u64_u32 v[46:47], vcc, s28, 1, v[2:3]
	global_load_dwordx4 v[46:49], v[46:47], off offset:1024
	v_mad_u64_u32 v[50:51], vcc, s29, 1, v[2:3]
	global_load_dwordx4 v[50:53], v[50:51], off
	v_mad_u64_u32 v[54:55], vcc, s30, 1, v[2:3]
	global_load_dwordx4 v[54:57], v[54:55], off offset:3072
	v_mad_u64_u32 v[58:59], vcc, s31, 1, v[2:3]
	global_load_dwordx4 v[58:61], v[58:59], off offset:2048
	v_mad_u64_u32 v[62:63], vcc, s34, 1, v[2:3]
	global_load_dwordx4 v[62:65], v[62:63], off offset:1024
	v_mad_u64_u32 v[66:67], vcc, s35, 1, v[2:3]
	global_load_dwordx4 v[66:69], v[66:67], off
	v_mad_u64_u32 v[70:71], vcc, s36, 1, v[2:3]
	global_load_dwordx4 v[70:73], v[70:71], off offset:3072
	v_mad_u64_u32 v[74:75], vcc, s37, 1, v[2:3]
	global_load_dwordx4 v[74:77], v[74:75], off offset:2048
	v_mad_u64_u32 v[78:79], vcc, s38, 1, v[2:3]
	global_load_dwordx4 v[78:81], v[78:79], off offset:1024
	v_mad_u64_u32 v[82:83], vcc, s39, 1, v[2:3]
	global_load_dwordx4 v[82:85], v[82:83], off
	v_mad_u64_u32 v[86:87], vcc, s40, 1, v[2:3]
	global_load_dwordx4 v[86:89], v[86:87], off offset:3072
	v_mad_u64_u32 v[90:91], vcc, s41, 1, v[2:3]
	global_load_dwordx4 v[90:93], v[90:91], off offset:2048
	v_mad_u64_u32 v[94:95], vcc, s42, 1, v[2:3]
	global_load_dwordx4 v[94:97], v[94:95], off offset:1024
	v_cmp_lt_i32_e32 vcc, v31, v32
	s_waitcnt vmcnt(0)
	v_max3_f32 v4, |v4|, |v38|, |v42|
	v_max3_f32 v4, v4, |v46|, |v50|
	v_max3_f32 v4, v4, |v54|, |v58|
	v_max3_f32 v4, v4, |v62|, |v66|
	v_max3_f32 v4, v4, |v70|, |v74|
	v_max3_f32 v4, v4, |v78|, |v82|
	v_max3_f32 v4, v4, |v86|, |v90|
	v_max3_f32 v5, |v5|, |v39|, |v43|
	v_max3_f32 v5, v5, |v47|, |v51|
	v_max3_f32 v5, v5, |v55|, |v59|
	v_max3_f32 v5, v5, |v63|, |v67|
	v_max3_f32 v5, v5, |v71|, |v75|
	v_max3_f32 v5, v5, |v79|, |v83|
	v_max3_f32 v5, v5, |v87|, |v91|
	v_max3_f32 v6, |v6|, |v40|, |v44|
	v_max3_f32 v6, v6, |v48|, |v52|
	v_max3_f32 v6, v6, |v56|, |v60|
	v_max3_f32 v6, v6, |v64|, |v68|
	v_max3_f32 v6, v6, |v72|, |v76|
	v_max3_f32 v6, v6, |v80|, |v84|
	v_max3_f32 v6, v6, |v88|, |v92|
	v_max3_f32 v7, |v7|, |v41|, |v45|
	v_max3_f32 v7, v7, |v49|, |v53|
	v_max3_f32 v7, v7, |v57|, |v61|
	v_max3_f32 v7, v7, |v65|, |v69|
	v_max3_f32 v7, v7, |v73|, |v77|
	v_max3_f32 v7, v7, |v81|, |v85|
	v_max3_f32 v7, v7, |v89|, |v93|
	v_max3_f32 v1, v4, |v94|, |v94|
	v_max3_f32 v3, v5, |v95|, |v95|
	v_max3_f32 v5, v6, |v96|, |v96|
	v_max3_f32 v7, v7, |v97|, |v97|
	v_cndmask_b32_e32 v2, v30, v31, vcc
	v_cmp_lt_i32_e32 vcc, v33, v32
	v_lshlrev_b32_e32 v8, 2, v2
	s_nop 0
	v_cndmask_b32_e32 v2, v30, v33, vcc
	v_cmp_lt_i32_e32 vcc, v34, v32
	v_lshlrev_b32_e32 v9, 2, v2
	s_nop 0
	v_cndmask_b32_e32 v2, v30, v34, vcc
	v_lshlrev_b32_e32 v38, 2, v2
	ds_bpermute_b32 v2, v8, v1
	ds_bpermute_b32 v4, v8, v3
	ds_bpermute_b32 v6, v8, v5
	ds_bpermute_b32 v8, v8, v7
	s_waitcnt lgkmcnt(3)
	v_max_f32_e32 v2, v2, v2
	s_waitcnt lgkmcnt(2)
	v_max_f32_e32 v4, v4, v4
	s_waitcnt lgkmcnt(1)
	v_max_f32_e32 v6, v6, v6
	s_waitcnt lgkmcnt(0)
	v_max_f32_e32 v8, v8, v8
	v_max_f32_e32 v1, v1, v2
	v_max_f32_e32 v3, v3, v4
	v_max_f32_e32 v5, v5, v6
	v_max_f32_e32 v7, v7, v8
	ds_bpermute_b32 v2, v9, v1
	ds_bpermute_b32 v4, v9, v3
	ds_bpermute_b32 v6, v9, v5
	ds_bpermute_b32 v8, v9, v7
	s_waitcnt lgkmcnt(3)
	v_max_f32_e32 v2, v2, v2
	s_waitcnt lgkmcnt(2)
	v_max_f32_e32 v4, v4, v4
	s_waitcnt lgkmcnt(1)
	v_max_f32_e32 v6, v6, v6
	s_waitcnt lgkmcnt(0)
	v_max_f32_e32 v8, v8, v8
	v_max_f32_e32 v1, v1, v2
	v_max_f32_e32 v3, v3, v4
	v_max_f32_e32 v5, v5, v6
	v_max_f32_e32 v7, v7, v8
	ds_bpermute_b32 v2, v38, v1
	ds_bpermute_b32 v4, v38, v3
	ds_bpermute_b32 v6, v38, v5
	ds_bpermute_b32 v8, v38, v7
	s_and_saveexec_b64 s[18:19], s[6:7]
	s_cbranch_execz .LBB0_518
	s_lshl_b32 s17, s69, 6
	s_and_b32 s17, s17, 0x3fff00
	s_cmpk_gt_u32 s8, 0x57f
	s_cselect_b32 s8, 0x80, 0
	v_mul_u32_u24_e32 v9, s21, v36
	s_or_b32 s8, s17, s8
	s_and_b32 s16, s16, 0x60
	v_lshlrev_b32_e32 v38, 2, v9
	v_mov_b32_e32 v39, v11
	s_or_b32 s8, s8, s16
	v_lshl_add_u64 v[38:39], s[10:11], 0, v[38:39]
	s_lshl_b32 s8, s8, 2
	s_waitcnt lgkmcnt(3)
	v_max_f32_e32 v2, v2, v2
	v_max_f32_e32 v1, v1, v1
	v_lshl_add_u64 v[38:39], v[38:39], 0, s[8:9]
	s_waitcnt lgkmcnt(2)
	v_max_f32_e32 v4, v4, v4
	v_max_f32_e32 v3, v3, v3
	v_max_f32_e32 v1, v1, v2
	s_waitcnt lgkmcnt(1)
	v_max_f32_e32 v6, v6, v6
	v_max_f32_e32 v5, v5, v5
	v_max_f32_e32 v3, v3, v4
	v_mul_f32_e32 v1, 0x3fb33333, v1
	v_readfirstlane_b32 s16, v38
	v_readfirstlane_b32 s17, v39
	s_waitcnt lgkmcnt(0)
	v_max_f32_e32 v8, v8, v8
	v_max_f32_e32 v7, v7, v7
	v_max_f32_e32 v5, v5, v6
	v_max_f32_e32 v7, v7, v8
	global_atomic_umax v29, v1, s[16:17]
	v_mul_f32_e32 v1, 0x3fb33333, v3
	global_atomic_umax v29, v1, s[16:17] offset:4
	v_mul_f32_e32 v1, 0x3fb33333, v5
	global_atomic_umax v29, v1, s[16:17] offset:8
	v_mul_f32_e32 v1, 0x3fb33333, v7
	global_atomic_umax v29, v1, s[16:17] offset:12

; __device__ __forceinline__ void colmax_item(const float* src, int ld, int k0, int c0, float* cmx  , int lane) {
;     const int c = lane & 7, q = lane >> 3;
;     f32x4 mx = (f32x4){0.f, 0.f, 0.f, 0.f};
; #pragma unroll
;     for (int g = 0; g < 4; ++g)
; #pragma unroll
;         for (int j = 0; j < 4; ++j) { const f32x4 v = *(const f32x4*)(src + (size_t)(k0 + 32 * g + 4 * q + j) * ld + c0 + 4 * c);
;             mx[0] = fmaxf(mx[0], fabsf(v[0])); mx[1] = fmaxf(mx[1], fabsf(v[1])); mx[2] = fmaxf(mx[2], fabsf(v[2])); mx[3] = fmaxf(mx[3], fabsf(v[3])); }
; #pragma unroll
;     for (int i = 0; i < 4; ++i) { float v = mx[i]; v = fmaxf(v, __shfl_xor(v, 8)); v = fmaxf(v, __shfl_xor(v, 16)); v = fmaxf(v, __shfl_xor(v, 32)); mx[i] = v; }
;     if (q == 0) {
; #pragma unroll
;         for (int i = 0; i < 4; ++i) atomicMax((unsigned*)(cmx + 4 * c + i), __float_as_uint(mx[i] * CMS_F)); }
; }
; template <int GRP>
; __device__ __forceinline__ void conv_item(Frame& F, int r) {
;     ...
;     else { constexpr int KBN = (GRP == 3) ? 16 : CMS_KB, I_E = KBN * 88; const int up = r / (8 * I_E); r %= (8 * I_E); const int e = r / I_E; r %= I_E; const int kb = r / 88, nb = r % 88, n0 = nb * 32, drow = (n0 >> 7) * 256 + up * 128 + (n0 & 127);
;         if (GRP == 3) cvt_item_i8(inptr(F, up ? IN_MU : IN_MG) + (size_t)e * D * DFE, DFE, kb * 128, n0, ws + WS_MGU + (size_t)e * 2 * DFE * D, D, drow, cmx + 2 * DFF + e * 2 * DFE + drow, scr, F.lane);
;         else colmax_item(inptr(F, up ? IN_MU : IN_MG) + (size_t)e * D * DFE, DFE, kb * 128, n0, cmx + 2 * DFF + e * 2 * DFE + drow, F.lane); }
.LBB0_631:
	s_cmpk_gt_i32 s20, 0x3ff
	s_mov_b64 s[16:17], -1
	s_cbranch_scc0 .LBB0_639
	s_cmpk_gt_u32 s20, 0x2fff
	s_cbranch_scc0 .LBB0_636
	s_add_i32 s8, s20, 0xffffd000
	s_add_i32 s16, s20, 0xca80
	s_cmpk_lt_u32 s8, 0x580
	s_cselect_b32 s16, s8, s16
	s_and_b32 s17, s16, 0xffff
	s_mul_i32 s17, s17, 0xba2f
	s_lshr_b32 s21, s17, 23
	s_mul_i32 s17, s21, 0xb0
	s_sub_i32 s16, s16, s17
	s_and_b32 s17, s16, 0xffff
	s_add_i32 s16, s17, 0xffffffa8
	s_min_u32 s67, s17, s16
	s_lshl_b32 s16, s67, 5
	s_cmpk_lt_u32 s20, 0x3580
	s_movk_i32 s18, 0xa0
	s_cselect_b32 s18, s18, 0xa8
	s_add_i32 s18, s18, 0
	s_add_i32 s18, s18, 0x20200
	v_mov_b32_e32 v1, s18
	s_waitcnt lgkmcnt(3)
	ds_read_b64 v[2:3], v1
	s_cmpk_gt_u32 s17, 0x57
	s_cselect_b32 s17, 0x80, 0
	v_or_b32_e32 v1, s17, v15
	s_ashr_i32 s17, s16, 31
	s_waitcnt lgkmcnt(0)
	v_readfirstlane_b32 s18, v2
	v_readfirstlane_b32 s19, v3
	v_mul_u32_u24_e32 v2, s21, v35
	v_mov_b32_e32 v3, v11
	v_lshlrev_b64 v[2:3], 2, v[2:3]
	v_lshl_add_u64 v[2:3], s[18:19], 0, v[2:3]
	s_lshl_b64 s[18:19], s[16:17], 2
	v_lshl_add_u64 v[2:3], v[2:3], 0, s[18:19]
	v_lshl_add_u64 v[2:3], v[2:3], 0, v[10:11]
	v_mul_u32_u24_e32 v4, 0x2c00, v1
	v_mov_b32_e32 v5, v11
	v_lshl_add_u64 v[2:3], v[2:3], 0, v[4:5]
	s_movk_i32 s17, 0x5000
	global_load_dwordx4 v[4:7], v[2:3], off
	v_mad_u64_u32 v[38:39], vcc, s25, 1, v[2:3]
	global_load_dwordx4 v[38:41], v[38:39], off offset:3072
	v_mad_u64_u32 v[42:43], vcc, s17, 1, v[2:3]
	global_load_dwordx4 v[42:45], v[42:43], off offset:2048
	v_mad_u64_u32 v[46:47], vcc, s26, 1, v[2:3]
	global_load_dwordx4 v[46:49], v[46:47], off offset:1024
	v_mad_u64_u32 v[50:51], vcc, s27, 1, v[2:3]
	global_load_dwordx4 v[50:53], v[50:51], off
	v_mad_u64_u32 v[54:55], vcc, s28, 1, v[2:3]
	global_load_dwordx4 v[54:57], v[54:55], off offset:3072
	v_mad_u64_u32 v[58:59], vcc, s29, 1, v[2:3]
	global_load_dwordx4 v[58:61], v[58:59], off offset:2048
	v_mad_u64_u32 v[62:63], vcc, s30, 1, v[2:3]
	global_load_dwordx4 v[62:65], v[62:63], off offset:1024
	v_mad_u64_u32 v[66:67], vcc, s31, 1, v[2:3]
	global_load_dwordx4 v[66:69], v[66:67], off
	v_mad_u64_u32 v[70:71], vcc, s34, 1, v[2:3]
	global_load_dwordx4 v[70:73], v[70:71], off offset:3072
	v_mad_u64_u32 v[74:75], vcc, s35, 1, v[2:3]
	global_load_dwordx4 v[74:77], v[74:75], off offset:2048
	v_mad_u64_u32 v[78:79], vcc, s36, 1, v[2:3]
	global_load_dwordx4 v[78:81], v[78:79], off offset:1024
	v_mad_u64_u32 v[82:83], vcc, s37, 1, v[2:3]
	global_load_dwordx4 v[82:85], v[82:83], off
	v_mad_u64_u32 v[86:87], vcc, s38, 1, v[2:3]
	global_load_dwordx4 v[86:89], v[86:87], off offset:3072
	v_mad_u64_u32 v[90:91], vcc, s39, 1, v[2:3]
	global_load_dwordx4 v[90:93], v[90:91], off offset:2048
	v_mad_u64_u32 v[94:95], vcc, s40, 1, v[2:3]
	global_load_dwordx4 v[94:97], v[94:95], off offset:1024
	v_cmp_lt_i32_e32 vcc, v31, v32
	s_waitcnt vmcnt(0)
	v_max3_f32 v4, |v4|, |v38|, |v42|
	v_max3_f32 v4, v4, |v46|, |v50|
	v_max3_f32 v4, v4, |v54|, |v58|
	v_max3_f32 v4, v4, |v62|, |v66|
	v_max3_f32 v4, v4, |v70|, |v74|
	v_max3_f32 v4, v4, |v78|, |v82|
	v_max3_f32 v4, v4, |v86|, |v90|
	v_max3_f32 v5, |v5|, |v39|, |v43|
	v_max3_f32 v5, v5, |v47|, |v51|
	v_max3_f32 v5, v5, |v55|, |v59|
	v_max3_f32 v5, v5, |v63|, |v67|
	v_max3_f32 v5, v5, |v71|, |v75|
	v_max3_f32 v5, v5, |v79|, |v83|
	v_max3_f32 v5, v5, |v87|, |v91|
	v_max3_f32 v6, |v6|, |v40|, |v44|
	v_max3_f32 v6, v6, |v48|, |v52|
	v_max3_f32 v6, v6, |v56|, |v60|
	v_max3_f32 v6, v6, |v64|, |v68|
	v_max3_f32 v6, v6, |v72|, |v76|
	v_max3_f32 v6, v6, |v80|, |v84|
	v_max3_f32 v6, v6, |v88|, |v92|
	v_max3_f32 v7, |v7|, |v41|, |v45|
	v_max3_f32 v7, v7, |v49|, |v53|
	v_max3_f32 v7, v7, |v57|, |v61|
	v_max3_f32 v7, v7, |v65|, |v69|
	v_max3_f32 v7, v7, |v73|, |v77|
	v_max3_f32 v7, v7, |v81|, |v85|
	v_max3_f32 v7, v7, |v89|, |v93|
	v_max3_f32 v1, v4, |v94|, |v94|
	v_max3_f32 v3, v5, |v95|, |v95|
	v_max3_f32 v5, v6, |v96|, |v96|
	v_max3_f32 v7, v7, |v97|, |v97|
	v_cndmask_b32_e32 v2, v30, v31, vcc
	v_cmp_lt_i32_e32 vcc, v33, v32
	v_lshlrev_b32_e32 v8, 2, v2
	s_nop 0
	v_cndmask_b32_e32 v2, v30, v33, vcc
	v_cmp_lt_i32_e32 vcc, v34, v32
	v_lshlrev_b32_e32 v9, 2, v2
	s_nop 0
	v_cndmask_b32_e32 v2, v30, v34, vcc
	v_lshlrev_b32_e32 v38, 2, v2
	ds_bpermute_b32 v2, v8, v1
	ds_bpermute_b32 v4, v8, v3
	ds_bpermute_b32 v6, v8, v5
	ds_bpermute_b32 v8, v8, v7
	s_waitcnt lgkmcnt(3)
	v_max_f32_e32 v2, v2, v2
	s_waitcnt lgkmcnt(2)
	v_max_f32_e32 v4, v4, v4
	s_waitcnt lgkmcnt(1)
	v_max_f32_e32 v6, v6, v6
	s_waitcnt lgkmcnt(0)
	v_max_f32_e32 v8, v8, v8
	v_max_f32_e32 v1, v1, v2
	v_max_f32_e32 v3, v3, v4
	v_max_f32_e32 v5, v5, v6
	v_max_f32_e32 v7, v7, v8
	ds_bpermute_b32 v2, v9, v1
	ds_bpermute_b32 v4, v9, v3
	ds_bpermute_b32 v6, v9, v5
	ds_bpermute_b32 v8, v9, v7
	s_waitcnt lgkmcnt(3)
	v_max_f32_e32 v2, v2, v2
	s_waitcnt lgkmcnt(2)
	v_max_f32_e32 v4, v4, v4
	s_waitcnt lgkmcnt(1)
	v_max_f32_e32 v6, v6, v6
	s_waitcnt lgkmcnt(0)
	v_max_f32_e32 v8, v8, v8
	v_max_f32_e32 v1, v1, v2
	v_max_f32_e32 v3, v3, v4
	v_max_f32_e32 v5, v5, v6
	v_max_f32_e32 v7, v7, v8
	ds_bpermute_b32 v2, v38, v1
	ds_bpermute_b32 v4, v38, v3
	ds_bpermute_b32 v6, v38, v5
	ds_bpermute_b32 v8, v38, v7
	s_and_saveexec_b64 s[18:19], s[6:7]
	s_cbranch_execz .LBB0_635
	s_lshl_b32 s17, s67, 6
	s_and_b32 s17, s17, 0x3fff00
	s_cmpk_gt_u32 s8, 0x57f
	s_cselect_b32 s8, 0x80, 0
	v_mul_u32_u24_e32 v9, s21, v36
	s_or_b32 s8, s17, s8
	s_and_b32 s16, s16, 0x60
	v_lshlrev_b32_e32 v38, 2, v9
	v_mov_b32_e32 v39, v11
	s_or_b32 s8, s8, s16
	v_lshl_add_u64 v[38:39], s[10:11], 0, v[38:39]
	s_lshl_b32 s8, s8, 2
	s_waitcnt lgkmcnt(3)
	v_max_f32_e32 v2, v2, v2
	v_max_f32_e32 v1, v1, v1
	v_lshl_add_u64 v[38:39], v[38:39], 0, s[8:9]
	s_waitcnt lgkmcnt(2)
	v_max_f32_e32 v4, v4, v4
	v_max_f32_e32 v3, v3, v3
	v_max_f32_e32 v1, v1, v2
	s_waitcnt lgkmcnt(1)
	v_max_f32_e32 v6, v6, v6
	v_max_f32_e32 v5, v5, v5
	v_max_f32_e32 v3, v3, v4
	v_mul_f32_e32 v1, 0x3fb33333, v1
	v_readfirstlane_b32 s16, v38
	v_readfirstlane_b32 s17, v39
	s_waitcnt lgkmcnt(0)
	v_max_f32_e32 v8, v8, v8
	v_max_f32_e32 v7, v7, v7
	v_max_f32_e32 v5, v5, v6
	v_max_f32_e32 v7, v7, v8
	global_atomic_umax v29, v1, s[16:17]
	v_mul_f32_e32 v1, 0x3fb33333, v3
	global_atomic_umax v29, v1, s[16:17] offset:4
	v_mul_f32_e32 v1, 0x3fb33333, v5
	global_atomic_umax v29, v1, s[16:17] offset:8
	v_mul_f32_e32 v1, 0x3fb33333, v7
	global_atomic_umax v29, v1, s[16:17] offset:12

; __device__ __forceinline__ void colmax_item(const float* src, int ld, int k0, int c0, float* cmx  , int lane) {
;     const int c = lane & 7, q = lane >> 3;
;     f32x4 mx = (f32x4){0.f, 0.f, 0.f, 0.f};
; #pragma unroll
;     for (int g = 0; g < 4; ++g)
; #pragma unroll
;         for (int j = 0; j < 4; ++j) { const f32x4 v = *(const f32x4*)(src + (size_t)(k0 + 32 * g + 4 * q + j) * ld + c0 + 4 * c);
;             mx[0] = fmaxf(mx[0], fabsf(v[0])); mx[1] = fmaxf(mx[1], fabsf(v[1])); mx[2] = fmaxf(mx[2], fabsf(v[2])); mx[3] = fmaxf(mx[3], fabsf(v[3])); }
; #pragma unroll
;     for (int i = 0; i < 4; ++i) { float v = mx[i]; v = fmaxf(v, __shfl_xor(v, 8)); v = fmaxf(v, __shfl_xor(v, 16)); v = fmaxf(v, __shfl_xor(v, 32)); mx[i] = v; }
;     if (q == 0) {
; #pragma unroll
;         for (int i = 0; i < 4; ++i) atomicMax((unsigned*)(cmx + 4 * c + i), __float_as_uint(mx[i] * CMS_F)); }
; }
; template <int GRP>
; __device__ __forceinline__ void conv_item(Frame& F, int r) {
;     ...
;     else { constexpr int KBN = (GRP == 3) ? 16 : CMS_KB, I_E = KBN * 88; const int up = r / (8 * I_E); r %= (8 * I_E); const int e = r / I_E; r %= I_E; const int kb = r / 88, nb = r % 88, n0 = nb * 32, drow = (n0 >> 7) * 256 + up * 128 + (n0 & 127);
;         if (GRP == 3) cvt_item_i8(inptr(F, up ? IN_MU : IN_MG) + (size_t)e * D * DFE, DFE, kb * 128, n0, ws + WS_MGU + (size_t)e * 2 * DFE * D, D, drow, cmx + 2 * DFF + e * 2 * DFE + drow, scr, F.lane);
;         else colmax_item(inptr(F, up ? IN_MU : IN_MG) + (size_t)e * D * DFE, DFE, kb * 128, n0, cmx + 2 * DFF + e * 2 * DFE + drow, F.lane); }
.LBB0_789:
	s_cmpk_gt_i32 s22, 0x3ff
	s_mov_b64 s[16:17], -1
	s_cbranch_scc0 .LBB0_797
	s_cmpk_gt_u32 s22, 0x2fff
	s_cbranch_scc0 .LBB0_794
	s_add_i32 s8, s22, 0xffffd000
	s_add_i32 s16, s22, 0xca80
	s_cmpk_lt_u32 s8, 0x580
	s_cselect_b32 s16, s8, s16
	s_and_b32 s17, s16, 0xffff
	s_mul_i32 s17, s17, 0xba2f
	s_lshr_b32 s23, s17, 23
	s_mul_i32 s17, s23, 0xb0
	s_sub_i32 s16, s16, s17
	s_and_b32 s17, s16, 0xffff
	s_add_i32 s16, s17, 0xffffffa8
	s_min_u32 s69, s17, s16
	s_lshl_b32 s16, s69, 5
	s_cmpk_lt_u32 s22, 0x3580
	s_movk_i32 s20, 0xa0
	s_cselect_b32 s20, s20, 0xa8
	s_add_i32 s20, s20, 0
	s_add_i32 s20, s20, 0x20200
	v_mov_b32_e32 v1, s20
	s_waitcnt lgkmcnt(3)
	ds_read_b64 v[2:3], v1
	s_cmpk_gt_u32 s17, 0x57
	s_cselect_b32 s17, 0x80, 0
	v_or_b32_e32 v1, s17, v15
	s_ashr_i32 s17, s16, 31
	s_waitcnt lgkmcnt(0)
	v_readfirstlane_b32 s20, v2
	v_readfirstlane_b32 s21, v3
	v_mul_u32_u24_e32 v2, s23, v35
	v_mov_b32_e32 v3, v11
	v_lshlrev_b64 v[2:3], 2, v[2:3]
	v_lshl_add_u64 v[2:3], s[20:21], 0, v[2:3]
	s_lshl_b64 s[20:21], s[16:17], 2
	v_lshl_add_u64 v[2:3], v[2:3], 0, s[20:21]
	v_lshl_add_u64 v[2:3], v[2:3], 0, v[10:11]
	v_mul_u32_u24_e32 v4, 0x2c00, v1
	v_mov_b32_e32 v5, v11
	v_lshl_add_u64 v[2:3], v[2:3], 0, v[4:5]
	s_movk_i32 s17, 0x5000
	global_load_dwordx4 v[4:7], v[2:3], off
	v_mad_u64_u32 v[38:39], vcc, s27, 1, v[2:3]
	global_load_dwordx4 v[38:41], v[38:39], off offset:3072
	v_mad_u64_u32 v[42:43], vcc, s17, 1, v[2:3]
	global_load_dwordx4 v[42:45], v[42:43], off offset:2048
	v_mad_u64_u32 v[46:47], vcc, s28, 1, v[2:3]
	global_load_dwordx4 v[46:49], v[46:47], off offset:1024
	v_mad_u64_u32 v[50:51], vcc, s29, 1, v[2:3]
	global_load_dwordx4 v[50:53], v[50:51], off
	v_mad_u64_u32 v[54:55], vcc, s30, 1, v[2:3]
	global_load_dwordx4 v[54:57], v[54:55], off offset:3072
	v_mad_u64_u32 v[58:59], vcc, s31, 1, v[2:3]
	global_load_dwordx4 v[58:61], v[58:59], off offset:2048
	v_mad_u64_u32 v[62:63], vcc, s34, 1, v[2:3]
	global_load_dwordx4 v[62:65], v[62:63], off offset:1024
	v_mad_u64_u32 v[66:67], vcc, s35, 1, v[2:3]
	global_load_dwordx4 v[66:69], v[66:67], off
	v_mad_u64_u32 v[70:71], vcc, s36, 1, v[2:3]
	global_load_dwordx4 v[70:73], v[70:71], off offset:3072
	v_mad_u64_u32 v[74:75], vcc, s37, 1, v[2:3]
	global_load_dwordx4 v[74:77], v[74:75], off offset:2048
	v_mad_u64_u32 v[78:79], vcc, s38, 1, v[2:3]
	global_load_dwordx4 v[78:81], v[78:79], off offset:1024
	v_mad_u64_u32 v[82:83], vcc, s39, 1, v[2:3]
	global_load_dwordx4 v[82:85], v[82:83], off
	v_mad_u64_u32 v[86:87], vcc, s40, 1, v[2:3]
	global_load_dwordx4 v[86:89], v[86:87], off offset:3072
	v_mad_u64_u32 v[90:91], vcc, s41, 1, v[2:3]
	global_load_dwordx4 v[90:93], v[90:91], off offset:2048
	v_mad_u64_u32 v[94:95], vcc, s42, 1, v[2:3]
	global_load_dwordx4 v[94:97], v[94:95], off offset:1024
	v_cmp_lt_i32_e32 vcc, v31, v32
	s_waitcnt vmcnt(0)
	v_max3_f32 v4, |v4|, |v38|, |v42|
	v_max3_f32 v4, v4, |v46|, |v50|
	v_max3_f32 v4, v4, |v54|, |v58|
	v_max3_f32 v4, v4, |v62|, |v66|
	v_max3_f32 v4, v4, |v70|, |v74|
	v_max3_f32 v4, v4, |v78|, |v82|
	v_max3_f32 v4, v4, |v86|, |v90|
	v_max3_f32 v5, |v5|, |v39|, |v43|
	v_max3_f32 v5, v5, |v47|, |v51|
	v_max3_f32 v5, v5, |v55|, |v59|
	v_max3_f32 v5, v5, |v63|, |v67|
	v_max3_f32 v5, v5, |v71|, |v75|
	v_max3_f32 v5, v5, |v79|, |v83|
	v_max3_f32 v5, v5, |v87|, |v91|
	v_max3_f32 v6, |v6|, |v40|, |v44|
	v_max3_f32 v6, v6, |v48|, |v52|
	v_max3_f32 v6, v6, |v56|, |v60|
	v_max3_f32 v6, v6, |v64|, |v68|
	v_max3_f32 v6, v6, |v72|, |v76|
	v_max3_f32 v6, v6, |v80|, |v84|
	v_max3_f32 v6, v6, |v88|, |v92|
	v_max3_f32 v7, |v7|, |v41|, |v45|
	v_max3_f32 v7, v7, |v49|, |v53|
	v_max3_f32 v7, v7, |v57|, |v61|
	v_max3_f32 v7, v7, |v65|, |v69|
	v_max3_f32 v7, v7, |v73|, |v77|
	v_max3_f32 v7, v7, |v81|, |v85|
	v_max3_f32 v7, v7, |v89|, |v93|
	v_max3_f32 v1, v4, |v94|, |v94|
	v_max3_f32 v3, v5, |v95|, |v95|
	v_max3_f32 v5, v6, |v96|, |v96|
	v_max3_f32 v7, v7, |v97|, |v97|
	v_cndmask_b32_e32 v2, v30, v31, vcc
	v_cmp_lt_i32_e32 vcc, v33, v32
	v_lshlrev_b32_e32 v8, 2, v2
	s_nop 0
	v_cndmask_b32_e32 v2, v30, v33, vcc
	v_cmp_lt_i32_e32 vcc, v34, v32
	v_lshlrev_b32_e32 v9, 2, v2
	s_nop 0
	v_cndmask_b32_e32 v2, v30, v34, vcc
	v_lshlrev_b32_e32 v38, 2, v2
	ds_bpermute_b32 v2, v8, v1
	ds_bpermute_b32 v4, v8, v3
	ds_bpermute_b32 v6, v8, v5
	ds_bpermute_b32 v8, v8, v7
	s_waitcnt lgkmcnt(3)
	v_max_f32_e32 v2, v2, v2
	s_waitcnt lgkmcnt(2)
	v_max_f32_e32 v4, v4, v4
	s_waitcnt lgkmcnt(1)
	v_max_f32_e32 v6, v6, v6
	s_waitcnt lgkmcnt(0)
	v_max_f32_e32 v8, v8, v8
	v_max_f32_e32 v1, v1, v2
	v_max_f32_e32 v3, v3, v4
	v_max_f32_e32 v5, v5, v6
	v_max_f32_e32 v7, v7, v8
	ds_bpermute_b32 v2, v9, v1
	ds_bpermute_b32 v4, v9, v3
	ds_bpermute_b32 v6, v9, v5
	ds_bpermute_b32 v8, v9, v7
	s_waitcnt lgkmcnt(3)
	v_max_f32_e32 v2, v2, v2
	s_waitcnt lgkmcnt(2)
	v_max_f32_e32 v4, v4, v4
	s_waitcnt lgkmcnt(1)
	v_max_f32_e32 v6, v6, v6
	s_waitcnt lgkmcnt(0)
	v_max_f32_e32 v8, v8, v8
	v_max_f32_e32 v1, v1, v2
	v_max_f32_e32 v3, v3, v4
	v_max_f32_e32 v5, v5, v6
	v_max_f32_e32 v7, v7, v8
	ds_bpermute_b32 v2, v38, v1
	ds_bpermute_b32 v4, v38, v3
	ds_bpermute_b32 v6, v38, v5
	ds_bpermute_b32 v8, v38, v7
	s_and_saveexec_b64 s[20:21], s[6:7]
	s_cbranch_execz .LBB0_793
	s_lshl_b32 s17, s69, 6
	s_and_b32 s17, s17, 0x3fff00
	s_cmpk_gt_u32 s8, 0x57f
	s_cselect_b32 s8, 0x80, 0
	v_mul_u32_u24_e32 v9, s23, v36
	s_or_b32 s8, s17, s8
	s_and_b32 s16, s16, 0x60
	v_lshlrev_b32_e32 v38, 2, v9
	v_mov_b32_e32 v39, v11
	s_or_b32 s8, s8, s16
	v_lshl_add_u64 v[38:39], s[10:11], 0, v[38:39]
	s_lshl_b32 s8, s8, 2
	s_waitcnt lgkmcnt(3)
	v_max_f32_e32 v2, v2, v2
	v_max_f32_e32 v1, v1, v1
	v_lshl_add_u64 v[38:39], v[38:39], 0, s[8:9]
	s_waitcnt lgkmcnt(2)
	v_max_f32_e32 v4, v4, v4
	v_max_f32_e32 v3, v3, v3
	v_max_f32_e32 v1, v1, v2
	s_waitcnt lgkmcnt(1)
	v_max_f32_e32 v6, v6, v6
	v_max_f32_e32 v5, v5, v5
	v_max_f32_e32 v3, v3, v4
	v_mul_f32_e32 v1, 0x3fb33333, v1
	v_readfirstlane_b32 s16, v38
	v_readfirstlane_b32 s17, v39
	s_waitcnt lgkmcnt(0)
	v_max_f32_e32 v8, v8, v8
	v_max_f32_e32 v7, v7, v7
	v_max_f32_e32 v5, v5, v6
	v_max_f32_e32 v7, v7, v8
	global_atomic_umax v29, v1, s[16:17]
	v_mul_f32_e32 v1, 0x3fb33333, v3
	global_atomic_umax v29, v1, s[16:17] offset:4
	v_mul_f32_e32 v1, 0x3fb33333, v5
	global_atomic_umax v29, v1, s[16:17] offset:8
	v_mul_f32_e32 v1, 0x3fb33333, v7
	global_atomic_umax v29, v1, s[16:17] offset:12
